# EpiSwiglu8 epilogues (dense-up, MoE-up) rewritten by hand: packed muls, x16 folded into sigmoid denominator via fma, trans/VALU interleave, incremental store addresses
# speedup vs baseline: 1.0043x; 1.0043x over previous
.LBB0_648:
	s_and_b32 s11, s4, 3
	s_mov_b64 s[4:5], 0x80
	s_add_i32 m0, s1, 0x18000
	v_lshl_add_u64 v[8:9], v[8:9], 0, s[4:5]
	s_lshl_b32 s7, s10, 13
	s_lshl_b32 s22, s11, 12
	s_waitcnt vmcnt(2)
	s_barrier
	global_load_lds_dwordx4 v[8:9], off
	v_lshl_add_u64 v[6:7], v[6:7], 0, s[4:5]
	s_add_i32 m0, s1, 0x1a000
	s_add_i32 s47, s1, 0x8000
	s_add_i32 s50, s1, 0xa000
	global_load_lds_dwordx4 v[6:7], off
	v_lshl_add_u64 v[2:3], v[2:3], 0, s[4:5]
	s_mov_b32 m0, s47
	s_add_u32 s20, s28, 0x40080
	global_load_lds_dwordx4 v[2:3], off
	v_lshl_add_u64 v[2:3], v[4:5], 0, s[4:5]
	s_mov_b32 m0, s50
	s_addc_u32 s21, s29, 0
	global_load_lds_dwordx4 v[2:3], off
	s_add_i32 m0, s1, 0x1c000
	v_lshl_add_u64 v[2:3], s[20:21], 0, v[134:135]
	global_load_lds_dwordx4 v[2:3], off
	v_lshl_add_u64 v[2:3], s[20:21], 0, v[130:131]
	s_add_i32 m0, s1, 0x1e000
	s_cmpk_lt_u32 s6, 0x100
	global_load_lds_dwordx4 v[2:3], off
	v_and_b32_e32 v2, 15, v1
	v_lshrrev_b32_e32 v3, 1, v1
	v_and_b32_e32 v3, 24, v3
	v_lshlrev_b32_e32 v4, 6, v2
	v_lshl_or_b32 v4, v3, 1, v4
	v_lshl_or_b32 v146, s10, 6, v2
	v_lshl_or_b32 v2, s11, 5, v3
	v_mov_b32_e32 v3, v135
	v_lshl_add_u64 v[2:3], s[8:9], 0, v[2:3]
	s_mov_b64 s[8:9], 0x19a00000
	v_lshl_add_u64 v[138:139], v[2:3], 0, s[8:9]
	v_lshlrev_b32_e32 v2, 14, v14
	v_and_b32_e32 v2, 0xffff8000, v2
	v_lshl_add_u32 v2, v13, 11, v2
	v_and_b32_e32 v3, 1, v14
	v_lshl_or_b32 v2, v3, 6, v2
	v_lshl_add_u32 v140, v15, 1, v2
	v_lshlrev_b32_e32 v2, 14, v10
	v_lshlrev_b32_e32 v1, 2, v1
	v_and_b32_e32 v2, 0xffff8000, v2
	v_and_b32_e32 v1, 32, v1
	s_waitcnt vmcnt(6)
	v_lshl_add_u32 v2, v11, 11, v2
	v_and_b32_e32 v3, 1, v10
	v_bitop3_b32 v5, v4, s7, v1 bitop3:0xde
	v_bitop3_b32 v1, v4, s22, v1 bitop3:0xde
	v_lshl_or_b32 v2, v3, 6, v2
	s_cselect_b64 s[6:7], -1, 0
	v_mov_b32_e32 v141, v135
	v_lshl_add_u32 v142, v12, 1, v2
	v_mov_b32_e32 v143, v135
	v_add_u32_e32 v147, s41, v1
	v_add_u32_e32 v148, s48, v1
	v_add_u32_e32 v149, 0, v5
	s_mov_b32 s8, 0x3d800000
	s_mov_b32 s9, 0xc3e00000
	s_movk_i32 s51, 0xb00
	v_mov_b32_e32 v150, 0x43e00000
	s_mov_b32 s53, s42
	s_mov_b32 s55, s0
	s_barrier
	s_waitcnt vmcnt(0)
	s_branch .LBB0_651

.LBB0_657:
	s_lshl_b32 s26, s53, 7
	s_ashr_i32 s27, s26, 31
	v_lshl_add_u32 v151, s55, 8, v146
	s_mov_b32 s98, 0xbfb8aa3b
	v_lshl_add_u64 v[144:145], v[138:139], 0, s[26:27]
	s_mov_b32 s101, 0
	v_mad_i64_i32 v[144:145], s[26:27], v151, s51, v[144:145]
	v_pk_mul_f32 v[152:153], v[126:127], s[98:99] op_sel_hi:[1,0]
	v_pk_mul_f32 v[154:155], v[128:129], s[98:99] op_sel_hi:[1,0]
	v_exp_f32_e32 v152, v152
	v_pk_mul_f32 v[156:157], v[122:123], s[98:99] op_sel_hi:[1,0]
	v_pk_mul_f32 v[158:159], v[124:125], s[98:99] op_sel_hi:[1,0]
	v_exp_f32_e32 v153, v153
	v_pk_mul_f32 v[164:165], v[110:111], s[98:99] op_sel_hi:[1,0]
	v_pk_mul_f32 v[166:167], v[112:113], s[98:99] op_sel_hi:[1,0]
	v_exp_f32_e32 v154, v154
	v_pk_mul_f32 v[168:169], v[106:107], s[98:99] op_sel_hi:[1,0]
	v_pk_fma_f32 v[152:153], v[152:153], s[8:9], s[8:9] op_sel_hi:[1,0,0]
	v_exp_f32_e32 v155, v155
	v_pk_mul_f32 v[170:171], v[108:109], s[98:99] op_sel_hi:[1,0]
	s_mul_i32 s100, s51, 0x10
	v_exp_f32_e32 v156, v156
	v_lshl_add_u64 v[174:175], s[100:101], 0, v[144:145]
	v_pk_fma_f32 v[154:155], v[154:155], s[8:9], s[8:9] op_sel_hi:[1,0,0]
	v_exp_f32_e32 v157, v157
	v_pk_mul_f32 v[176:177], v[94:95], s[98:99] op_sel_hi:[1,0]
	v_pk_mul_f32 v[178:179], v[96:97], s[98:99] op_sel_hi:[1,0]
	v_exp_f32_e32 v158, v158
	v_pk_mul_f32 v[180:181], v[90:91], s[98:99] op_sel_hi:[1,0]
	v_pk_fma_f32 v[156:157], v[156:157], s[8:9], s[8:9] op_sel_hi:[1,0,0]
	v_exp_f32_e32 v159, v159
	v_pk_mul_f32 v[182:183], v[92:93], s[98:99] op_sel_hi:[1,0]
	s_mul_i32 s100, s51, 0x20
	v_rcp_f32_e32 v152, v152
	v_lshl_add_u64 v[186:187], s[100:101], 0, v[144:145]
	v_pk_fma_f32 v[158:159], v[158:159], s[8:9], s[8:9] op_sel_hi:[1,0,0]
	v_rcp_f32_e32 v153, v153
	v_pk_mul_f32 v[188:189], v[78:79], s[98:99] op_sel_hi:[1,0]
	v_pk_mul_f32 v[190:191], v[80:81], s[98:99] op_sel_hi:[1,0]
	v_rcp_f32_e32 v154, v154
	v_pk_mul_f32 v[192:193], v[74:75], s[98:99] op_sel_hi:[1,0]
	v_pk_mul_f32 v[152:153], v[126:127], v[152:153]
	v_rcp_f32_e32 v155, v155
	v_pk_mul_f32 v[152:153], v[152:153], v[118:119]
	v_pk_mul_f32 v[194:195], v[76:77], s[98:99] op_sel_hi:[1,0]
	v_rcp_f32_e32 v156, v156
	v_med3_f32 v152, v152, s9, v150
	v_pk_mul_f32 v[154:155], v[128:129], v[154:155]
	v_rcp_f32_e32 v157, v157
	v_pk_mul_f32 v[154:155], v[154:155], v[120:121]
	v_med3_f32 v153, v153, s9, v150
	v_rcp_f32_e32 v158, v158
	v_med3_f32 v154, v154, s9, v150
	v_pk_mul_f32 v[156:157], v[122:123], v[156:157]
	v_rcp_f32_e32 v159, v159
	v_pk_mul_f32 v[156:157], v[156:157], v[114:115]
	v_med3_f32 v155, v155, s9, v150
	v_exp_f32_e32 v164, v164
	v_med3_f32 v156, v156, s9, v150
	v_pk_mul_f32 v[158:159], v[124:125], v[158:159]
	v_exp_f32_e32 v165, v165
	v_pk_mul_f32 v[158:159], v[158:159], v[116:117]
	v_med3_f32 v157, v157, s9, v150
	v_exp_f32_e32 v166, v166
	v_med3_f32 v158, v158, s9, v150
	v_med3_f32 v159, v159, s9, v150
	v_exp_f32_e32 v167, v167
	v_cvt_pk_fp8_f32 v160, v152, v153
	v_cvt_pk_fp8_f32 v161, v156, v157
	v_exp_f32_e32 v168, v168
	v_cvt_pk_fp8_f32 v160, v154, v155 op_sel:[0,0,1]
	v_cvt_pk_fp8_f32 v161, v158, v159 op_sel:[0,0,1]
	v_exp_f32_e32 v169, v169
	global_store_dwordx2 v[144:145], v[160:161], off
	v_pk_fma_f32 v[164:165], v[164:165], s[8:9], s[8:9] op_sel_hi:[1,0,0]
	v_exp_f32_e32 v170, v170
	v_pk_fma_f32 v[166:167], v[166:167], s[8:9], s[8:9] op_sel_hi:[1,0,0]
	v_pk_fma_f32 v[168:169], v[168:169], s[8:9], s[8:9] op_sel_hi:[1,0,0]
	v_exp_f32_e32 v171, v171
	s_mul_i32 s100, s51, 0x30
	v_pk_mul_f32 v[152:153], v[62:63], s[98:99] op_sel_hi:[1,0]
	v_rcp_f32_e32 v164, v164
	v_lshl_add_u64 v[198:199], s[100:101], 0, v[144:145]
	v_pk_fma_f32 v[170:171], v[170:171], s[8:9], s[8:9] op_sel_hi:[1,0,0]
	v_rcp_f32_e32 v165, v165
	v_pk_mul_f32 v[154:155], v[64:65], s[98:99] op_sel_hi:[1,0]
	v_pk_mul_f32 v[156:157], v[58:59], s[98:99] op_sel_hi:[1,0]
	v_rcp_f32_e32 v166, v166
	v_pk_mul_f32 v[158:159], v[60:61], s[98:99] op_sel_hi:[1,0]
	v_pk_mul_f32 v[164:165], v[110:111], v[164:165]
	v_rcp_f32_e32 v167, v167
	v_pk_mul_f32 v[164:165], v[164:165], v[102:103]
	v_rcp_f32_e32 v168, v168
	v_med3_f32 v164, v164, s9, v150
	v_med3_f32 v165, v165, s9, v150
	v_rcp_f32_e32 v169, v169
	v_pk_mul_f32 v[166:167], v[112:113], v[166:167]
	v_cvt_pk_fp8_f32 v172, v164, v165
	v_rcp_f32_e32 v170, v170
	v_pk_mul_f32 v[166:167], v[166:167], v[104:105]
	v_pk_mul_f32 v[168:169], v[106:107], v[168:169]
	v_rcp_f32_e32 v171, v171
	v_pk_mul_f32 v[168:169], v[168:169], v[98:99]
	v_med3_f32 v166, v166, s9, v150
	v_exp_f32_e32 v176, v176
	v_med3_f32 v167, v167, s9, v150
	v_pk_mul_f32 v[170:171], v[108:109], v[170:171]
	v_exp_f32_e32 v177, v177
	v_pk_mul_f32 v[170:171], v[170:171], v[100:101]
	v_med3_f32 v168, v168, s9, v150
	v_exp_f32_e32 v178, v178
	v_med3_f32 v169, v169, s9, v150
	v_med3_f32 v170, v170, s9, v150
	v_exp_f32_e32 v179, v179
	v_med3_f32 v171, v171, s9, v150
	v_cvt_pk_fp8_f32 v173, v168, v169
	v_exp_f32_e32 v180, v180
	v_cvt_pk_fp8_f32 v172, v166, v167 op_sel:[0,0,1]
	v_cvt_pk_fp8_f32 v173, v170, v171 op_sel:[0,0,1]
	v_exp_f32_e32 v181, v181
	global_store_dwordx2 v[174:175], v[172:173], off
	v_pk_fma_f32 v[176:177], v[176:177], s[8:9], s[8:9] op_sel_hi:[1,0,0]
	v_exp_f32_e32 v182, v182
	v_pk_fma_f32 v[178:179], v[178:179], s[8:9], s[8:9] op_sel_hi:[1,0,0]
	v_pk_fma_f32 v[180:181], v[180:181], s[8:9], s[8:9] op_sel_hi:[1,0,0]
	v_exp_f32_e32 v183, v183
	s_mul_i32 s100, s51, 0x80
	v_pk_mul_f32 v[164:165], v[46:47], s[98:99] op_sel_hi:[1,0]
	v_rcp_f32_e32 v176, v176
	v_lshl_add_u64 v[162:163], s[100:101], 0, v[144:145]
	v_pk_fma_f32 v[182:183], v[182:183], s[8:9], s[8:9] op_sel_hi:[1,0,0]
	v_rcp_f32_e32 v177, v177
	v_pk_mul_f32 v[166:167], v[48:49], s[98:99] op_sel_hi:[1,0]
	v_pk_mul_f32 v[168:169], v[42:43], s[98:99] op_sel_hi:[1,0]
	v_rcp_f32_e32 v178, v178
	v_pk_mul_f32 v[170:171], v[44:45], s[98:99] op_sel_hi:[1,0]
	v_pk_mul_f32 v[176:177], v[94:95], v[176:177]
	v_rcp_f32_e32 v179, v179
	v_pk_mul_f32 v[176:177], v[176:177], v[86:87]
	v_rcp_f32_e32 v180, v180
	v_med3_f32 v176, v176, s9, v150
	v_med3_f32 v177, v177, s9, v150
	v_rcp_f32_e32 v181, v181
	v_pk_mul_f32 v[178:179], v[96:97], v[178:179]
	v_cvt_pk_fp8_f32 v184, v176, v177
	v_rcp_f32_e32 v182, v182
	v_pk_mul_f32 v[178:179], v[178:179], v[88:89]
	v_pk_mul_f32 v[180:181], v[90:91], v[180:181]
	v_rcp_f32_e32 v183, v183
	v_pk_mul_f32 v[180:181], v[180:181], v[82:83]
	v_med3_f32 v178, v178, s9, v150
	v_exp_f32_e32 v188, v188
	v_med3_f32 v179, v179, s9, v150
	v_pk_mul_f32 v[182:183], v[92:93], v[182:183]
	v_exp_f32_e32 v189, v189
	v_pk_mul_f32 v[182:183], v[182:183], v[84:85]
	v_med3_f32 v180, v180, s9, v150
	v_exp_f32_e32 v190, v190
	v_med3_f32 v181, v181, s9, v150
	v_med3_f32 v182, v182, s9, v150
	v_exp_f32_e32 v191, v191
	v_med3_f32 v183, v183, s9, v150
	v_cvt_pk_fp8_f32 v185, v180, v181
	v_exp_f32_e32 v192, v192
	v_cvt_pk_fp8_f32 v184, v178, v179 op_sel:[0,0,1]
	v_cvt_pk_fp8_f32 v185, v182, v183 op_sel:[0,0,1]
	v_exp_f32_e32 v193, v193
	global_store_dwordx2 v[186:187], v[184:185], off
	v_pk_fma_f32 v[188:189], v[188:189], s[8:9], s[8:9] op_sel_hi:[1,0,0]
	v_exp_f32_e32 v194, v194
	v_pk_fma_f32 v[190:191], v[190:191], s[8:9], s[8:9] op_sel_hi:[1,0,0]
	v_pk_fma_f32 v[192:193], v[192:193], s[8:9], s[8:9] op_sel_hi:[1,0,0]
	v_exp_f32_e32 v195, v195
	s_mul_i32 s100, s51, 0x90
	v_pk_mul_f32 v[176:177], v[30:31], s[98:99] op_sel_hi:[1,0]
	v_rcp_f32_e32 v188, v188
	v_lshl_add_u64 v[174:175], s[100:101], 0, v[144:145]
	v_pk_fma_f32 v[194:195], v[194:195], s[8:9], s[8:9] op_sel_hi:[1,0,0]
	v_rcp_f32_e32 v189, v189
	v_pk_mul_f32 v[178:179], v[32:33], s[98:99] op_sel_hi:[1,0]
	v_pk_mul_f32 v[180:181], v[26:27], s[98:99] op_sel_hi:[1,0]
	v_rcp_f32_e32 v190, v190
	v_pk_mul_f32 v[182:183], v[28:29], s[98:99] op_sel_hi:[1,0]
	v_pk_mul_f32 v[188:189], v[78:79], v[188:189]
	v_rcp_f32_e32 v191, v191
	v_pk_mul_f32 v[188:189], v[188:189], v[70:71]
	v_rcp_f32_e32 v192, v192
	v_med3_f32 v188, v188, s9, v150
	v_med3_f32 v189, v189, s9, v150
	v_rcp_f32_e32 v193, v193
	v_pk_mul_f32 v[190:191], v[80:81], v[190:191]
	v_cvt_pk_fp8_f32 v196, v188, v189
	v_rcp_f32_e32 v194, v194
	v_pk_mul_f32 v[190:191], v[190:191], v[72:73]
	v_pk_mul_f32 v[192:193], v[74:75], v[192:193]
	v_rcp_f32_e32 v195, v195
	v_pk_mul_f32 v[192:193], v[192:193], v[66:67]
	v_med3_f32 v190, v190, s9, v150
	v_exp_f32_e32 v152, v152
	v_med3_f32 v191, v191, s9, v150
	v_pk_mul_f32 v[194:195], v[76:77], v[194:195]
	v_exp_f32_e32 v153, v153
	v_pk_mul_f32 v[194:195], v[194:195], v[68:69]
	v_med3_f32 v192, v192, s9, v150
	v_exp_f32_e32 v154, v154
	v_med3_f32 v193, v193, s9, v150
	v_med3_f32 v194, v194, s9, v150
	v_exp_f32_e32 v155, v155
	v_med3_f32 v195, v195, s9, v150
	v_cvt_pk_fp8_f32 v197, v192, v193
	v_exp_f32_e32 v156, v156
	v_cvt_pk_fp8_f32 v196, v190, v191 op_sel:[0,0,1]
	v_cvt_pk_fp8_f32 v197, v194, v195 op_sel:[0,0,1]
	v_exp_f32_e32 v157, v157
	global_store_dwordx2 v[198:199], v[196:197], off
	v_pk_fma_f32 v[152:153], v[152:153], s[8:9], s[8:9] op_sel_hi:[1,0,0]
	v_exp_f32_e32 v158, v158
	v_pk_fma_f32 v[154:155], v[154:155], s[8:9], s[8:9] op_sel_hi:[1,0,0]
	v_pk_fma_f32 v[156:157], v[156:157], s[8:9], s[8:9] op_sel_hi:[1,0,0]
	v_exp_f32_e32 v159, v159
	s_mul_i32 s100, s51, 0xa0
	v_pk_mul_f32 v[188:189], v[14:15], s[98:99] op_sel_hi:[1,0]
	v_rcp_f32_e32 v152, v152
	v_lshl_add_u64 v[186:187], s[100:101], 0, v[144:145]
	v_pk_fma_f32 v[158:159], v[158:159], s[8:9], s[8:9] op_sel_hi:[1,0,0]
	v_rcp_f32_e32 v153, v153
	v_pk_mul_f32 v[190:191], v[16:17], s[98:99] op_sel_hi:[1,0]
	v_pk_mul_f32 v[192:193], v[10:11], s[98:99] op_sel_hi:[1,0]
	v_rcp_f32_e32 v154, v154
	v_pk_mul_f32 v[194:195], v[12:13], s[98:99] op_sel_hi:[1,0]
	v_pk_mul_f32 v[152:153], v[62:63], v[152:153]
	v_rcp_f32_e32 v155, v155
	v_pk_mul_f32 v[152:153], v[152:153], v[54:55]
	v_rcp_f32_e32 v156, v156
	v_med3_f32 v152, v152, s9, v150
	v_med3_f32 v153, v153, s9, v150
	v_rcp_f32_e32 v157, v157
	v_pk_mul_f32 v[154:155], v[64:65], v[154:155]
	v_cvt_pk_fp8_f32 v160, v152, v153
	v_rcp_f32_e32 v158, v158
	v_pk_mul_f32 v[154:155], v[154:155], v[56:57]
	v_pk_mul_f32 v[156:157], v[58:59], v[156:157]
	v_rcp_f32_e32 v159, v159
	v_pk_mul_f32 v[156:157], v[156:157], v[50:51]
	v_med3_f32 v154, v154, s9, v150
	v_exp_f32_e32 v164, v164
	v_med3_f32 v155, v155, s9, v150
	v_pk_mul_f32 v[158:159], v[60:61], v[158:159]
	v_exp_f32_e32 v165, v165
	v_pk_mul_f32 v[158:159], v[158:159], v[52:53]
	v_med3_f32 v156, v156, s9, v150
	v_exp_f32_e32 v166, v166
	v_med3_f32 v157, v157, s9, v150
	v_med3_f32 v158, v158, s9, v150
	v_exp_f32_e32 v167, v167
	v_med3_f32 v159, v159, s9, v150
	v_cvt_pk_fp8_f32 v161, v156, v157
	v_exp_f32_e32 v168, v168
	v_cvt_pk_fp8_f32 v160, v154, v155 op_sel:[0,0,1]
	v_cvt_pk_fp8_f32 v161, v158, v159 op_sel:[0,0,1]
	v_exp_f32_e32 v169, v169
	global_store_dwordx2 v[162:163], v[160:161], off
	v_pk_fma_f32 v[164:165], v[164:165], s[8:9], s[8:9] op_sel_hi:[1,0,0]
	v_exp_f32_e32 v170, v170
	v_pk_fma_f32 v[166:167], v[166:167], s[8:9], s[8:9] op_sel_hi:[1,0,0]
	v_pk_fma_f32 v[168:169], v[168:169], s[8:9], s[8:9] op_sel_hi:[1,0,0]
	v_exp_f32_e32 v171, v171
	s_mul_i32 s100, s51, 0xb0
	v_rcp_f32_e32 v164, v164
	v_lshl_add_u64 v[198:199], s[100:101], 0, v[144:145]
	v_rcp_f32_e32 v165, v165
	v_pk_fma_f32 v[170:171], v[170:171], s[8:9], s[8:9] op_sel_hi:[1,0,0]
	v_rcp_f32_e32 v166, v166
	v_rcp_f32_e32 v167, v167
	v_rcp_f32_e32 v168, v168
	v_pk_mul_f32 v[164:165], v[46:47], v[164:165]
	v_rcp_f32_e32 v169, v169
	v_pk_mul_f32 v[164:165], v[164:165], v[38:39]
	v_pk_mul_f32 v[166:167], v[48:49], v[166:167]
	v_rcp_f32_e32 v170, v170
	v_pk_mul_f32 v[166:167], v[166:167], v[40:41]
	v_pk_mul_f32 v[168:169], v[42:43], v[168:169]
	v_rcp_f32_e32 v171, v171
	v_pk_mul_f32 v[168:169], v[168:169], v[34:35]
	v_med3_f32 v164, v164, s9, v150
	v_exp_f32_e32 v176, v176
	v_med3_f32 v165, v165, s9, v150
	v_pk_mul_f32 v[170:171], v[44:45], v[170:171]
	v_exp_f32_e32 v177, v177
	v_pk_mul_f32 v[170:171], v[170:171], v[36:37]
	v_med3_f32 v166, v166, s9, v150
	v_exp_f32_e32 v178, v178
	v_med3_f32 v167, v167, s9, v150
	v_med3_f32 v168, v168, s9, v150
	v_exp_f32_e32 v179, v179
	v_med3_f32 v169, v169, s9, v150
	v_med3_f32 v170, v170, s9, v150
	v_exp_f32_e32 v180, v180
	v_med3_f32 v171, v171, s9, v150
	v_cvt_pk_fp8_f32 v172, v164, v165
	v_exp_f32_e32 v181, v181
	v_cvt_pk_fp8_f32 v173, v168, v169
	v_cvt_pk_fp8_f32 v172, v166, v167 op_sel:[0,0,1]
	v_exp_f32_e32 v182, v182
	v_cvt_pk_fp8_f32 v173, v170, v171 op_sel:[0,0,1]
	v_pk_fma_f32 v[176:177], v[176:177], s[8:9], s[8:9] op_sel_hi:[1,0,0]
	v_exp_f32_e32 v183, v183
	global_store_dwordx2 v[174:175], v[172:173], off
	v_pk_fma_f32 v[178:179], v[178:179], s[8:9], s[8:9] op_sel_hi:[1,0,0]
	v_rcp_f32_e32 v176, v176
	v_pk_fma_f32 v[180:181], v[180:181], s[8:9], s[8:9] op_sel_hi:[1,0,0]
	v_pk_fma_f32 v[182:183], v[182:183], s[8:9], s[8:9] op_sel_hi:[1,0,0]
	v_rcp_f32_e32 v177, v177
	v_rcp_f32_e32 v178, v178
	v_rcp_f32_e32 v179, v179
	v_rcp_f32_e32 v180, v180
	v_rcp_f32_e32 v181, v181
	v_pk_mul_f32 v[176:177], v[30:31], v[176:177]
	v_rcp_f32_e32 v182, v182
	v_pk_mul_f32 v[178:179], v[32:33], v[178:179]
	v_pk_mul_f32 v[176:177], v[176:177], v[22:23]
	v_rcp_f32_e32 v183, v183
	v_pk_mul_f32 v[180:181], v[26:27], v[180:181]
	v_pk_mul_f32 v[178:179], v[178:179], v[24:25]
	v_exp_f32_e32 v188, v188
	v_pk_mul_f32 v[180:181], v[180:181], v[18:19]
	v_pk_mul_f32 v[182:183], v[28:29], v[182:183]
	v_exp_f32_e32 v189, v189
	v_pk_mul_f32 v[182:183], v[182:183], v[20:21]
	v_med3_f32 v176, v176, s9, v150
	v_exp_f32_e32 v190, v190
	v_med3_f32 v177, v177, s9, v150
	v_med3_f32 v178, v178, s9, v150
	v_exp_f32_e32 v191, v191
	v_med3_f32 v179, v179, s9, v150
	v_med3_f32 v180, v180, s9, v150
	v_exp_f32_e32 v192, v192
	v_med3_f32 v181, v181, s9, v150
	v_med3_f32 v182, v182, s9, v150
	v_exp_f32_e32 v193, v193
	v_med3_f32 v183, v183, s9, v150
	v_cvt_pk_fp8_f32 v184, v176, v177
	v_exp_f32_e32 v194, v194
	v_cvt_pk_fp8_f32 v185, v180, v181
	v_cvt_pk_fp8_f32 v184, v178, v179 op_sel:[0,0,1]
	v_exp_f32_e32 v195, v195
	v_cvt_pk_fp8_f32 v185, v182, v183 op_sel:[0,0,1]
	v_pk_fma_f32 v[188:189], v[188:189], s[8:9], s[8:9] op_sel_hi:[1,0,0]
	global_store_dwordx2 v[186:187], v[184:185], off
	v_rcp_f32_e32 v188, v188
	v_pk_fma_f32 v[190:191], v[190:191], s[8:9], s[8:9] op_sel_hi:[1,0,0]
	v_pk_fma_f32 v[192:193], v[192:193], s[8:9], s[8:9] op_sel_hi:[1,0,0]
	v_rcp_f32_e32 v189, v189
	v_pk_fma_f32 v[194:195], v[194:195], s[8:9], s[8:9] op_sel_hi:[1,0,0]
	v_rcp_f32_e32 v190, v190
	v_rcp_f32_e32 v191, v191
	v_rcp_f32_e32 v192, v192
	v_pk_mul_f32 v[188:189], v[14:15], v[188:189]
	v_rcp_f32_e32 v193, v193
	v_pk_mul_f32 v[188:189], v[188:189], v[6:7]
	v_pk_mul_f32 v[190:191], v[16:17], v[190:191]
	v_rcp_f32_e32 v194, v194
	v_pk_mul_f32 v[190:191], v[190:191], v[8:9]
	v_pk_mul_f32 v[192:193], v[10:11], v[192:193]
	v_rcp_f32_e32 v195, v195
	v_pk_mul_f32 v[192:193], v[192:193], v[2:3]
	v_med3_f32 v188, v188, s9, v150
	v_med3_f32 v189, v189, s9, v150
	v_med3_f32 v190, v190, s9, v150
	v_pk_mul_f32 v[194:195], v[12:13], v[194:195]
	v_med3_f32 v191, v191, s9, v150
	v_pk_mul_f32 v[194:195], v[194:195], v[4:5]
	v_med3_f32 v192, v192, s9, v150
	v_med3_f32 v193, v193, s9, v150
	v_med3_f32 v194, v194, s9, v150
	v_med3_f32 v195, v195, s9, v150
	v_cvt_pk_fp8_f32 v196, v188, v189
	v_cvt_pk_fp8_f32 v197, v192, v193
	v_cvt_pk_fp8_f32 v196, v190, v191 op_sel:[0,0,1]
	v_cvt_pk_fp8_f32 v197, v194, v195 op_sel:[0,0,1]
	s_nop 0
	global_store_dwordx2 v[198:199], v[196:197], off
	s_cmp_eq_u32 s46, 10
	s_mov_b64 s[26:27], -1
	s_cbranch_scc1 .LBB0_650
	s_andn2_b64 vcc, exec, s[2:3]
	s_cbranch_vccnz .LBB0_649
	s_barrier
	s_branch .LBB0_649

.LBB0_1305:
	v_writelane_b32 v254, s28, 44
	s_nop 1
	v_writelane_b32 v254, s29, 45
	v_writelane_b32 v254, s24, 46
	s_nop 1
	v_writelane_b32 v254, s25, 47
	v_writelane_b32 v254, s36, 48
	s_nop 1
	v_writelane_b32 v254, s37, 49
	s_or_b64 exec, exec, s[2:3]
	s_mov_b32 s0, 0
	s_waitcnt lgkmcnt(0)
	s_barrier
	s_add_u32 s2, s94, s0
	s_addc_u32 s3, s95, 0
	s_mov_b32 s52, s51
	v_readlane_b32 s67, v254, 22
	v_mov_b32_e32 v8, 0x10000
	global_load_dword v1, v8, s[2:3] sc1
	global_load_dword v2, v8, s[2:3] offset:256 sc1
	global_load_dword v3, v8, s[2:3] offset:512 sc1
	global_load_dword v4, v8, s[2:3] offset:768 sc1
	global_load_dword v5, v8, s[2:3] offset:1024 sc1
	global_load_dword v6, v8, s[2:3] offset:1280 sc1
	global_load_dword v7, v8, s[2:3] offset:1536 sc1
	s_nop 0
	global_load_dword v8, v8, s[2:3] offset:1792 sc1
	s_mov_b32 s50, 0
	s_waitcnt vmcnt(7)
	v_readfirstlane_b32 s0, v1
	s_waitcnt vmcnt(6)
	v_readfirstlane_b32 s1, v2
	s_waitcnt vmcnt(5)
	v_readfirstlane_b32 s4, v3
	s_addk_i32 s0, 0xff
	s_addk_i32 s1, 0xff
	s_waitcnt vmcnt(4)
	v_readfirstlane_b32 s5, v4
	s_addk_i32 s4, 0xff
	s_and_b32 s10, s0, 0xffffff00
	s_and_b32 s1, s1, 0xffffff00
	s_waitcnt vmcnt(3)
	v_readfirstlane_b32 s6, v5
	s_addk_i32 s5, 0xff
	s_and_b32 s4, s4, 0xffffff00
	s_add_i32 s1, s1, s10
	s_waitcnt vmcnt(2)
	v_readfirstlane_b32 s7, v6
	s_addk_i32 s6, 0xff
	s_and_b32 s11, s5, 0xffffff00
	s_add_i32 s5, s4, s1
	s_waitcnt vmcnt(1)
	v_readfirstlane_b32 s8, v7
	s_addk_i32 s7, 0xff
	s_and_b32 s6, s6, 0xffffff00
	s_add_i32 s10, s11, s5
	s_waitcnt vmcnt(0)
	v_readfirstlane_b32 s9, v8
	s_addk_i32 s8, 0xff
	s_and_b32 s12, s7, 0xffffff00
	s_add_i32 s11, s6, s10
	s_addk_i32 s9, 0xff
	s_and_b32 s13, s8, 0xffffff00
	s_add_i32 s12, s12, s11
	s_and_b32 s7, s9, 0xffffff00
	s_add_i32 s13, s13, s12
	s_add_i32 s7, s7, s13
	s_ashr_i32 s65, s7, 15
	s_bfe_u32 s74, s7, 0x70008
	s_cmp_lg_u32 s74, 0
	s_cselect_b64 s[16:17], -1, 0
	s_cmp_lg_u64 s[16:17], 0
	v_cndmask_b32_e64 v1, 0, 1, s[16:17]
	s_addc_u32 s19, s65, 0
	v_readfirstlane_b32 s75, v1
	s_mov_b32 s4, 0
	s_cmp_gt_i32 s19, -1
	s_cbranch_scc0 .LBB0_1449
	s_add_u32 s77, s2, 0x10a00000
	s_addc_u32 s6, s3, 0
	s_ashr_i32 s7, s0, 8
	s_ashr_i32 s8, s1, 8
	s_ashr_i32 s9, s5, 8
	s_ashr_i32 s10, s10, 8
	s_ashr_i32 s11, s11, 8
	s_ashr_i32 s12, s12, 8
	s_ashr_i32 s13, s13, 8
	s_add_u32 s56, s2, 0x1fe00000
	s_mov_b32 s5, s50
	s_addc_u32 s57, s3, 0
	s_lshl_b64 s[0:1], s[4:5], 2
	s_add_u32 s0, s92, s0
	v_writelane_b32 v254, s0, 50
	s_addc_u32 s0, s93, s1
	v_writelane_b32 v254, s0, 51
	s_add_u32 s0, s2, 0x18e00000
	v_writelane_b32 v254, s0, 52
	s_addc_u32 s0, s3, 0
	s_add_u32 s58, s2, 0x9200000
	s_addc_u32 s59, s3, 0
	s_cmpk_lg_i32 s67, 0x100
	s_cselect_b64 s[30:31], -1, 0
	s_ashr_i32 s53, s52, 31
	v_writelane_b32 v254, s0, 53
	s_lshr_b32 s0, s53, 30
	s_add_i32 s0, s52, s0
	s_ashr_i32 s1, s0, 2
	s_and_b32 s0, s0, -4
	v_writelane_b32 v254, s1, 54
	s_sub_i32 s0, s52, s0
	v_writelane_b32 v254, s0, 55
	s_lshl_b32 s0, s52, 4
	s_and_b32 s18, s0, 0x70
	s_ashr_i32 s0, s52, 4
	s_add_i32 s18, s18, s0
	s_lshr_b32 s0, s52, 2
	s_and_b32 s0, s0, 2
	s_ashr_i32 s20, s67, 31
	v_writelane_b32 v254, s0, 56
	s_or_b32 s0, s0, 1
	s_add_u32 s62, s2, 0x6000000
	s_addc_u32 s63, s3, 0
	s_add_u32 s22, s2, 0x2200000
	v_writelane_b32 v254, s0, 4
	s_addc_u32 s23, s3, 0
	s_bfe_i32 s0, s52, 0x10003
	s_and_b32 s24, s52, 8
	s_and_b32 s0, s0, 14
	v_writelane_b32 v254, s0, 57
	s_add_u32 s0, s2, 0x6000080
	s_addc_u32 s1, s3, 0
	v_writelane_b32 v254, s0, 58
	s_cmp_eq_u32 s96, 15
	s_movk_i32 s2, 0xe00
	v_writelane_b32 v254, s1, 59
	s_cselect_b64 s[0:1], -1, 0
	v_writelane_b32 v254, s0, 60
	s_cmp_eq_u32 s96, 14
	s_mov_b32 s3, 0xe0000
	v_writelane_b32 v254, s1, 61
	s_cselect_b64 s[0:1], -1, 0
	v_writelane_b32 v254, s0, 62
	s_cmp_eq_u32 s96, 13
	v_mov_b32_e32 v200, 0x7a7a7a7a
	v_writelane_b32 v254, s1, 63
	s_cselect_b64 s[0:1], -1, 0
	v_writelane_b32 v255, s0, 0
	s_cmp_eq_u32 s96, 12
	v_mov_b32_e32 v195, 0
	v_writelane_b32 v255, s1, 1
	s_cselect_b64 s[0:1], -1, 0
	v_writelane_b32 v255, s0, 2
	s_cmp_eq_u32 s96, 11
	s_movk_i32 s27, 0x7fff
	v_writelane_b32 v255, s1, 3
	s_cselect_b64 s[0:1], -1, 0
	v_writelane_b32 v255, s0, 4
	s_cmp_eq_u32 s96, 10
	s_mov_b32 s28, 0xffff0000
	v_writelane_b32 v255, s1, 5
	s_cselect_b64 s[0:1], -1, 0
	v_writelane_b32 v255, s0, 6
	s_cmp_eq_u32 s96, 9
	s_mov_b32 s66, 0x3d800000
	v_writelane_b32 v255, s1, 7
	s_cselect_b64 s[0:1], -1, 0
	v_writelane_b32 v255, s0, 8
	s_cmp_eq_u32 s96, 8
	s_mov_b32 s29, 0xc3e00000
	v_writelane_b32 v255, s1, 9
	s_cselect_b64 s[0:1], -1, 0
	v_writelane_b32 v255, s0, 10
	s_cmp_eq_u32 s96, 7
	v_mov_b32_e32 v201, 1
	v_writelane_b32 v255, s1, 11
	s_cselect_b64 s[0:1], -1, 0
	v_writelane_b32 v255, s0, 12
	s_cmp_eq_u32 s96, 6
	v_mov_b32_e32 v1, 0x43e00000
	v_writelane_b32 v255, s1, 13
	s_cselect_b64 s[0:1], -1, 0
	v_writelane_b32 v255, s0, 14
	s_cmp_eq_u32 s96, 5
	s_mov_b32 s35, 0
	v_writelane_b32 v255, s1, 15
	s_cselect_b64 s[0:1], -1, 0
	v_writelane_b32 v255, s0, 16
	s_cmp_eq_u32 s96, 4
	s_nop 0
	v_writelane_b32 v255, s1, 17
	s_cselect_b64 s[0:1], -1, 0
	v_writelane_b32 v255, s0, 18
	s_cmp_eq_u32 s96, 3
	s_nop 0
	v_writelane_b32 v255, s1, 19
	s_cselect_b64 s[0:1], -1, 0
	v_writelane_b32 v255, s0, 20
	s_cmp_eq_u32 s96, 2
	s_nop 0
	v_writelane_b32 v255, s1, 21
	s_cselect_b64 s[0:1], -1, 0
	v_writelane_b32 v255, s0, 22
	s_cmp_eq_u32 s96, 1
	s_nop 0
	v_writelane_b32 v255, s1, 23
	s_cselect_b64 s[0:1], -1, 0
	v_writelane_b32 v255, s0, 24
	s_cmp_eq_u32 s96, 0
	s_nop 0
	v_writelane_b32 v255, s1, 25
	s_cselect_b64 s[0:1], -1, 0
	v_writelane_b32 v255, s0, 26
	s_nop 1
	v_writelane_b32 v255, s1, 27
	s_add_i32 s1, 0, 0x20160
	s_lshl_b32 s0, s96, 6
	v_writelane_b32 v255, s1, 28
	s_add_i32 s1, 0, 0x20164
	v_writelane_b32 v255, s1, 29
	s_lshl_b32 s0, s0, 2
	v_writelane_b32 v255, s0, 30
	v_writelane_b32 v255, s92, 31
	s_nop 1
	v_writelane_b32 v255, s93, 32
	v_writelane_b32 v255, s94, 33
	v_writelane_b32 v255, s95, 34
	v_writelane_b32 v255, s16, 35
	s_nop 1
	v_writelane_b32 v255, s17, 36
	v_writelane_b32 v255, s19, 37
	v_writelane_b32 v255, s30, 38
	s_nop 1
	v_writelane_b32 v255, s31, 39
	v_writelane_b32 v255, s65, 40
	v_writelane_b32 v255, s74, 41
	v_writelane_b32 v255, s75, 42
	s_branch .LBB0_1309

.LBB0_1393:
	s_lshl_b32 s38, s42, 8
	v_mov_b32_e32 v2, v0
	s_add_i32 s38, s38, s31
	s_mov_b32 s98, 0xbfb8aa3b
	v_and_or_b32 v4, v2, 15, s38
	s_lshl_b32 s38, s45, 7
	s_ashr_i32 s39, s38, 31
	v_lshrrev_b32_e32 v2, 1, v2
	s_add_u32 s38, s5, s38
	v_and_or_b32 v194, v2, 24, s25
	s_addc_u32 s39, s4, s39
	v_lshl_add_u64 v[2:3], s[38:39], 0, v[194:195]
	s_andn2_b64 vcc, exec, s[92:93]
	s_mov_b32 s101, 0
	v_mad_i64_i32 v[2:3], s[38:39], v4, s2, v[2:3]
	v_pk_mul_f32 v[6:7], v[190:191], s[98:99] op_sel_hi:[1,0]
	v_pk_mul_f32 v[8:9], v[192:193], s[98:99] op_sel_hi:[1,0]
	v_exp_f32_e32 v6, v6
	v_pk_mul_f32 v[10:11], v[182:183], s[98:99] op_sel_hi:[1,0]
	v_pk_mul_f32 v[12:13], v[184:185], s[98:99] op_sel_hi:[1,0]
	v_exp_f32_e32 v7, v7
	v_pk_mul_f32 v[18:19], v[174:175], s[98:99] op_sel_hi:[1,0]
	v_pk_mul_f32 v[20:21], v[176:177], s[98:99] op_sel_hi:[1,0]
	v_exp_f32_e32 v8, v8
	v_pk_mul_f32 v[22:23], v[166:167], s[98:99] op_sel_hi:[1,0]
	v_pk_fma_f32 v[6:7], v[6:7], s[66:67], s[66:67] op_sel_hi:[1,0,0]
	v_exp_f32_e32 v9, v9
	v_pk_mul_f32 v[24:25], v[168:169], s[98:99] op_sel_hi:[1,0]
	s_mul_i32 s100, s2, 0x10
	v_exp_f32_e32 v10, v10
	v_lshl_add_u64 v[28:29], s[100:101], 0, v[2:3]
	v_pk_fma_f32 v[8:9], v[8:9], s[66:67], s[66:67] op_sel_hi:[1,0,0]
	v_exp_f32_e32 v11, v11
	v_pk_mul_f32 v[30:31], v[158:159], s[98:99] op_sel_hi:[1,0]
	v_pk_mul_f32 v[32:33], v[160:161], s[98:99] op_sel_hi:[1,0]
	v_exp_f32_e32 v12, v12
	v_pk_mul_f32 v[34:35], v[150:151], s[98:99] op_sel_hi:[1,0]
	v_pk_fma_f32 v[10:11], v[10:11], s[66:67], s[66:67] op_sel_hi:[1,0,0]
	v_exp_f32_e32 v13, v13
	v_pk_mul_f32 v[36:37], v[152:153], s[98:99] op_sel_hi:[1,0]
	s_mul_i32 s100, s2, 0x20
	v_rcp_f32_e32 v6, v6
	v_lshl_add_u64 v[40:41], s[100:101], 0, v[2:3]
	v_pk_fma_f32 v[12:13], v[12:13], s[66:67], s[66:67] op_sel_hi:[1,0,0]
	v_rcp_f32_e32 v7, v7
	v_pk_mul_f32 v[42:43], v[142:143], s[98:99] op_sel_hi:[1,0]
	v_pk_mul_f32 v[44:45], v[144:145], s[98:99] op_sel_hi:[1,0]
	v_rcp_f32_e32 v8, v8
	v_pk_mul_f32 v[46:47], v[134:135], s[98:99] op_sel_hi:[1,0]
	v_pk_mul_f32 v[6:7], v[190:191], v[6:7]
	v_rcp_f32_e32 v9, v9
	v_pk_mul_f32 v[6:7], v[6:7], v[186:187]
	v_pk_mul_f32 v[48:49], v[136:137], s[98:99] op_sel_hi:[1,0]
	v_rcp_f32_e32 v10, v10
	v_med3_f32 v6, v6, s29, v1
	v_pk_mul_f32 v[8:9], v[192:193], v[8:9]
	v_rcp_f32_e32 v11, v11
	v_pk_mul_f32 v[8:9], v[8:9], v[188:189]
	v_med3_f32 v7, v7, s29, v1
	v_rcp_f32_e32 v12, v12
	v_med3_f32 v8, v8, s29, v1
	v_pk_mul_f32 v[10:11], v[182:183], v[10:11]
	v_rcp_f32_e32 v13, v13
	v_pk_mul_f32 v[10:11], v[10:11], v[178:179]
	v_med3_f32 v9, v9, s29, v1
	v_exp_f32_e32 v18, v18
	v_med3_f32 v10, v10, s29, v1
	v_pk_mul_f32 v[12:13], v[184:185], v[12:13]
	v_exp_f32_e32 v19, v19
	v_pk_mul_f32 v[12:13], v[12:13], v[180:181]
	v_med3_f32 v11, v11, s29, v1
	v_exp_f32_e32 v20, v20
	v_med3_f32 v12, v12, s29, v1
	v_med3_f32 v13, v13, s29, v1
	v_exp_f32_e32 v21, v21
	v_cvt_pk_fp8_f32 v14, v6, v7
	v_cvt_pk_fp8_f32 v15, v10, v11
	v_exp_f32_e32 v22, v22
	v_cvt_pk_fp8_f32 v14, v8, v9 op_sel:[0,0,1]
	v_cvt_pk_fp8_f32 v15, v12, v13 op_sel:[0,0,1]
	v_exp_f32_e32 v23, v23
	global_store_dwordx2 v[2:3], v[14:15], off
	v_pk_fma_f32 v[18:19], v[18:19], s[66:67], s[66:67] op_sel_hi:[1,0,0]
	v_exp_f32_e32 v24, v24
	v_pk_fma_f32 v[20:21], v[20:21], s[66:67], s[66:67] op_sel_hi:[1,0,0]
	v_pk_fma_f32 v[22:23], v[22:23], s[66:67], s[66:67] op_sel_hi:[1,0,0]
	v_exp_f32_e32 v25, v25
	s_mul_i32 s100, s2, 0x30
	v_pk_mul_f32 v[6:7], v[126:127], s[98:99] op_sel_hi:[1,0]
	v_rcp_f32_e32 v18, v18
	v_lshl_add_u64 v[52:53], s[100:101], 0, v[2:3]
	v_pk_fma_f32 v[24:25], v[24:25], s[66:67], s[66:67] op_sel_hi:[1,0,0]
	v_rcp_f32_e32 v19, v19
	v_pk_mul_f32 v[8:9], v[128:129], s[98:99] op_sel_hi:[1,0]
	v_pk_mul_f32 v[10:11], v[118:119], s[98:99] op_sel_hi:[1,0]
	v_rcp_f32_e32 v20, v20
	v_pk_mul_f32 v[12:13], v[120:121], s[98:99] op_sel_hi:[1,0]
	v_pk_mul_f32 v[18:19], v[174:175], v[18:19]
	v_rcp_f32_e32 v21, v21
	v_pk_mul_f32 v[18:19], v[18:19], v[170:171]
	v_rcp_f32_e32 v22, v22
	v_med3_f32 v18, v18, s29, v1
	v_med3_f32 v19, v19, s29, v1
	v_rcp_f32_e32 v23, v23
	v_pk_mul_f32 v[20:21], v[176:177], v[20:21]
	v_cvt_pk_fp8_f32 v26, v18, v19
	v_rcp_f32_e32 v24, v24
	v_pk_mul_f32 v[20:21], v[20:21], v[172:173]
	v_pk_mul_f32 v[22:23], v[166:167], v[22:23]
	v_rcp_f32_e32 v25, v25
	v_pk_mul_f32 v[22:23], v[22:23], v[162:163]
	v_med3_f32 v20, v20, s29, v1
	v_exp_f32_e32 v30, v30
	v_med3_f32 v21, v21, s29, v1
	v_pk_mul_f32 v[24:25], v[168:169], v[24:25]
	v_exp_f32_e32 v31, v31
	v_pk_mul_f32 v[24:25], v[24:25], v[164:165]
	v_med3_f32 v22, v22, s29, v1
	v_exp_f32_e32 v32, v32
	v_med3_f32 v23, v23, s29, v1
	v_med3_f32 v24, v24, s29, v1
	v_exp_f32_e32 v33, v33
	v_med3_f32 v25, v25, s29, v1
	v_cvt_pk_fp8_f32 v27, v22, v23
	v_exp_f32_e32 v34, v34
	v_cvt_pk_fp8_f32 v26, v20, v21 op_sel:[0,0,1]
	v_cvt_pk_fp8_f32 v27, v24, v25 op_sel:[0,0,1]
	v_exp_f32_e32 v35, v35
	global_store_dwordx2 v[28:29], v[26:27], off
	v_pk_fma_f32 v[30:31], v[30:31], s[66:67], s[66:67] op_sel_hi:[1,0,0]
	v_exp_f32_e32 v36, v36
	v_pk_fma_f32 v[32:33], v[32:33], s[66:67], s[66:67] op_sel_hi:[1,0,0]
	v_pk_fma_f32 v[34:35], v[34:35], s[66:67], s[66:67] op_sel_hi:[1,0,0]
	v_exp_f32_e32 v37, v37
	s_mul_i32 s100, s2, 0x80
	v_pk_mul_f32 v[18:19], v[110:111], s[98:99] op_sel_hi:[1,0]
	v_rcp_f32_e32 v30, v30
	v_lshl_add_u64 v[16:17], s[100:101], 0, v[2:3]
	v_pk_fma_f32 v[36:37], v[36:37], s[66:67], s[66:67] op_sel_hi:[1,0,0]
	v_rcp_f32_e32 v31, v31
	v_pk_mul_f32 v[20:21], v[112:113], s[98:99] op_sel_hi:[1,0]
	v_pk_mul_f32 v[22:23], v[102:103], s[98:99] op_sel_hi:[1,0]
	v_rcp_f32_e32 v32, v32
	v_pk_mul_f32 v[24:25], v[104:105], s[98:99] op_sel_hi:[1,0]
	v_pk_mul_f32 v[30:31], v[158:159], v[30:31]
	v_rcp_f32_e32 v33, v33
	v_pk_mul_f32 v[30:31], v[30:31], v[154:155]
	v_rcp_f32_e32 v34, v34
	v_med3_f32 v30, v30, s29, v1
	v_med3_f32 v31, v31, s29, v1
	v_rcp_f32_e32 v35, v35
	v_pk_mul_f32 v[32:33], v[160:161], v[32:33]
	v_cvt_pk_fp8_f32 v38, v30, v31
	v_rcp_f32_e32 v36, v36
	v_pk_mul_f32 v[32:33], v[32:33], v[156:157]
	v_pk_mul_f32 v[34:35], v[150:151], v[34:35]
	v_rcp_f32_e32 v37, v37
	v_pk_mul_f32 v[34:35], v[34:35], v[146:147]
	v_med3_f32 v32, v32, s29, v1
	v_exp_f32_e32 v42, v42
	v_med3_f32 v33, v33, s29, v1
	v_pk_mul_f32 v[36:37], v[152:153], v[36:37]
	v_exp_f32_e32 v43, v43
	v_pk_mul_f32 v[36:37], v[36:37], v[148:149]
	v_med3_f32 v34, v34, s29, v1
	v_exp_f32_e32 v44, v44
	v_med3_f32 v35, v35, s29, v1
	v_med3_f32 v36, v36, s29, v1
	v_exp_f32_e32 v45, v45
	v_med3_f32 v37, v37, s29, v1
	v_cvt_pk_fp8_f32 v39, v34, v35
	v_exp_f32_e32 v46, v46
	v_cvt_pk_fp8_f32 v38, v32, v33 op_sel:[0,0,1]
	v_cvt_pk_fp8_f32 v39, v36, v37 op_sel:[0,0,1]
	v_exp_f32_e32 v47, v47
	global_store_dwordx2 v[40:41], v[38:39], off
	v_pk_fma_f32 v[42:43], v[42:43], s[66:67], s[66:67] op_sel_hi:[1,0,0]
	v_exp_f32_e32 v48, v48
	v_pk_fma_f32 v[44:45], v[44:45], s[66:67], s[66:67] op_sel_hi:[1,0,0]
	v_pk_fma_f32 v[46:47], v[46:47], s[66:67], s[66:67] op_sel_hi:[1,0,0]
	v_exp_f32_e32 v49, v49
	s_mul_i32 s100, s2, 0x90
	v_pk_mul_f32 v[30:31], v[94:95], s[98:99] op_sel_hi:[1,0]
	v_rcp_f32_e32 v42, v42
	v_lshl_add_u64 v[28:29], s[100:101], 0, v[2:3]
	v_pk_fma_f32 v[48:49], v[48:49], s[66:67], s[66:67] op_sel_hi:[1,0,0]
	v_rcp_f32_e32 v43, v43
	v_pk_mul_f32 v[32:33], v[96:97], s[98:99] op_sel_hi:[1,0]
	v_pk_mul_f32 v[34:35], v[86:87], s[98:99] op_sel_hi:[1,0]
	v_rcp_f32_e32 v44, v44
	v_pk_mul_f32 v[36:37], v[88:89], s[98:99] op_sel_hi:[1,0]
	v_pk_mul_f32 v[42:43], v[142:143], v[42:43]
	v_rcp_f32_e32 v45, v45
	v_pk_mul_f32 v[42:43], v[42:43], v[138:139]
	v_rcp_f32_e32 v46, v46
	v_med3_f32 v42, v42, s29, v1
	v_med3_f32 v43, v43, s29, v1
	v_rcp_f32_e32 v47, v47
	v_pk_mul_f32 v[44:45], v[144:145], v[44:45]
	v_cvt_pk_fp8_f32 v50, v42, v43
	v_rcp_f32_e32 v48, v48
	v_pk_mul_f32 v[44:45], v[44:45], v[140:141]
	v_pk_mul_f32 v[46:47], v[134:135], v[46:47]
	v_rcp_f32_e32 v49, v49
	v_pk_mul_f32 v[46:47], v[46:47], v[130:131]
	v_med3_f32 v44, v44, s29, v1
	v_exp_f32_e32 v6, v6
	v_med3_f32 v45, v45, s29, v1
	v_pk_mul_f32 v[48:49], v[136:137], v[48:49]
	v_exp_f32_e32 v7, v7
	v_pk_mul_f32 v[48:49], v[48:49], v[132:133]
	v_med3_f32 v46, v46, s29, v1
	v_exp_f32_e32 v8, v8
	v_med3_f32 v47, v47, s29, v1
	v_med3_f32 v48, v48, s29, v1
	v_exp_f32_e32 v9, v9
	v_med3_f32 v49, v49, s29, v1
	v_cvt_pk_fp8_f32 v51, v46, v47
	v_exp_f32_e32 v10, v10
	v_cvt_pk_fp8_f32 v50, v44, v45 op_sel:[0,0,1]
	v_cvt_pk_fp8_f32 v51, v48, v49 op_sel:[0,0,1]
	v_exp_f32_e32 v11, v11
	global_store_dwordx2 v[52:53], v[50:51], off
	v_pk_fma_f32 v[6:7], v[6:7], s[66:67], s[66:67] op_sel_hi:[1,0,0]
	v_exp_f32_e32 v12, v12
	v_pk_fma_f32 v[8:9], v[8:9], s[66:67], s[66:67] op_sel_hi:[1,0,0]
	v_pk_fma_f32 v[10:11], v[10:11], s[66:67], s[66:67] op_sel_hi:[1,0,0]
	v_exp_f32_e32 v13, v13
	s_mul_i32 s100, s2, 0xa0
	v_pk_mul_f32 v[42:43], v[78:79], s[98:99] op_sel_hi:[1,0]
	v_rcp_f32_e32 v6, v6
	v_lshl_add_u64 v[40:41], s[100:101], 0, v[2:3]
	v_pk_fma_f32 v[12:13], v[12:13], s[66:67], s[66:67] op_sel_hi:[1,0,0]
	v_rcp_f32_e32 v7, v7
	v_pk_mul_f32 v[44:45], v[80:81], s[98:99] op_sel_hi:[1,0]
	v_pk_mul_f32 v[46:47], v[70:71], s[98:99] op_sel_hi:[1,0]
	v_rcp_f32_e32 v8, v8
	v_pk_mul_f32 v[48:49], v[72:73], s[98:99] op_sel_hi:[1,0]
	v_pk_mul_f32 v[6:7], v[126:127], v[6:7]
	v_rcp_f32_e32 v9, v9
	v_pk_mul_f32 v[6:7], v[6:7], v[122:123]
	v_rcp_f32_e32 v10, v10
	v_med3_f32 v6, v6, s29, v1
	v_med3_f32 v7, v7, s29, v1
	v_rcp_f32_e32 v11, v11
	v_pk_mul_f32 v[8:9], v[128:129], v[8:9]
	v_cvt_pk_fp8_f32 v14, v6, v7
	v_rcp_f32_e32 v12, v12
	v_pk_mul_f32 v[8:9], v[8:9], v[124:125]
	v_pk_mul_f32 v[10:11], v[118:119], v[10:11]
	v_rcp_f32_e32 v13, v13
	v_pk_mul_f32 v[10:11], v[10:11], v[114:115]
	v_med3_f32 v8, v8, s29, v1
	v_exp_f32_e32 v18, v18
	v_med3_f32 v9, v9, s29, v1
	v_pk_mul_f32 v[12:13], v[120:121], v[12:13]
	v_exp_f32_e32 v19, v19
	v_pk_mul_f32 v[12:13], v[12:13], v[116:117]
	v_med3_f32 v10, v10, s29, v1
	v_exp_f32_e32 v20, v20
	v_med3_f32 v11, v11, s29, v1
	v_med3_f32 v12, v12, s29, v1
	v_exp_f32_e32 v21, v21
	v_med3_f32 v13, v13, s29, v1
	v_cvt_pk_fp8_f32 v15, v10, v11
	v_exp_f32_e32 v22, v22
	v_cvt_pk_fp8_f32 v14, v8, v9 op_sel:[0,0,1]
	v_cvt_pk_fp8_f32 v15, v12, v13 op_sel:[0,0,1]
	v_exp_f32_e32 v23, v23
	global_store_dwordx2 v[16:17], v[14:15], off
	v_pk_fma_f32 v[18:19], v[18:19], s[66:67], s[66:67] op_sel_hi:[1,0,0]
	v_exp_f32_e32 v24, v24
	v_pk_fma_f32 v[20:21], v[20:21], s[66:67], s[66:67] op_sel_hi:[1,0,0]
	v_pk_fma_f32 v[22:23], v[22:23], s[66:67], s[66:67] op_sel_hi:[1,0,0]
	v_exp_f32_e32 v25, v25
	s_mul_i32 s100, s2, 0xb0
	v_rcp_f32_e32 v18, v18
	v_lshl_add_u64 v[52:53], s[100:101], 0, v[2:3]
	v_rcp_f32_e32 v19, v19
	v_pk_fma_f32 v[24:25], v[24:25], s[66:67], s[66:67] op_sel_hi:[1,0,0]
	v_rcp_f32_e32 v20, v20
	v_rcp_f32_e32 v21, v21
	v_rcp_f32_e32 v22, v22
	v_pk_mul_f32 v[18:19], v[110:111], v[18:19]
	v_rcp_f32_e32 v23, v23
	v_pk_mul_f32 v[18:19], v[18:19], v[106:107]
	v_pk_mul_f32 v[20:21], v[112:113], v[20:21]
	v_rcp_f32_e32 v24, v24
	v_pk_mul_f32 v[20:21], v[20:21], v[108:109]
	v_pk_mul_f32 v[22:23], v[102:103], v[22:23]
	v_rcp_f32_e32 v25, v25
	v_pk_mul_f32 v[22:23], v[22:23], v[98:99]
	v_med3_f32 v18, v18, s29, v1
	v_exp_f32_e32 v30, v30
	v_med3_f32 v19, v19, s29, v1
	v_pk_mul_f32 v[24:25], v[104:105], v[24:25]
	v_exp_f32_e32 v31, v31
	v_pk_mul_f32 v[24:25], v[24:25], v[100:101]
	v_med3_f32 v20, v20, s29, v1
	v_exp_f32_e32 v32, v32
	v_med3_f32 v21, v21, s29, v1
	v_med3_f32 v22, v22, s29, v1
	v_exp_f32_e32 v33, v33
	v_med3_f32 v23, v23, s29, v1
	v_med3_f32 v24, v24, s29, v1
	v_exp_f32_e32 v34, v34
	v_med3_f32 v25, v25, s29, v1
	v_cvt_pk_fp8_f32 v26, v18, v19
	v_exp_f32_e32 v35, v35
	v_cvt_pk_fp8_f32 v27, v22, v23
	v_cvt_pk_fp8_f32 v26, v20, v21 op_sel:[0,0,1]
	v_exp_f32_e32 v36, v36
	v_cvt_pk_fp8_f32 v27, v24, v25 op_sel:[0,0,1]
	v_pk_fma_f32 v[30:31], v[30:31], s[66:67], s[66:67] op_sel_hi:[1,0,0]
	v_exp_f32_e32 v37, v37
	global_store_dwordx2 v[28:29], v[26:27], off
	v_pk_fma_f32 v[32:33], v[32:33], s[66:67], s[66:67] op_sel_hi:[1,0,0]
	v_rcp_f32_e32 v30, v30
	v_pk_fma_f32 v[34:35], v[34:35], s[66:67], s[66:67] op_sel_hi:[1,0,0]
	v_pk_fma_f32 v[36:37], v[36:37], s[66:67], s[66:67] op_sel_hi:[1,0,0]
	v_rcp_f32_e32 v31, v31
	v_rcp_f32_e32 v32, v32
	v_rcp_f32_e32 v33, v33
	v_rcp_f32_e32 v34, v34
	v_rcp_f32_e32 v35, v35
	v_pk_mul_f32 v[30:31], v[94:95], v[30:31]
	v_rcp_f32_e32 v36, v36
	v_pk_mul_f32 v[32:33], v[96:97], v[32:33]
	v_pk_mul_f32 v[30:31], v[30:31], v[90:91]
	v_rcp_f32_e32 v37, v37
	v_pk_mul_f32 v[34:35], v[86:87], v[34:35]
	v_pk_mul_f32 v[32:33], v[32:33], v[92:93]
	v_exp_f32_e32 v42, v42
	v_pk_mul_f32 v[34:35], v[34:35], v[82:83]
	v_pk_mul_f32 v[36:37], v[88:89], v[36:37]
	v_exp_f32_e32 v43, v43
	v_pk_mul_f32 v[36:37], v[36:37], v[84:85]
	v_med3_f32 v30, v30, s29, v1
	v_exp_f32_e32 v44, v44
	v_med3_f32 v31, v31, s29, v1
	v_med3_f32 v32, v32, s29, v1
	v_exp_f32_e32 v45, v45
	v_med3_f32 v33, v33, s29, v1
	v_med3_f32 v34, v34, s29, v1
	v_exp_f32_e32 v46, v46
	v_med3_f32 v35, v35, s29, v1
	v_med3_f32 v36, v36, s29, v1
	v_exp_f32_e32 v47, v47
	v_med3_f32 v37, v37, s29, v1
	v_cvt_pk_fp8_f32 v38, v30, v31
	v_exp_f32_e32 v48, v48
	v_cvt_pk_fp8_f32 v39, v34, v35
	v_cvt_pk_fp8_f32 v38, v32, v33 op_sel:[0,0,1]
	v_exp_f32_e32 v49, v49
	v_cvt_pk_fp8_f32 v39, v36, v37 op_sel:[0,0,1]
	v_pk_fma_f32 v[42:43], v[42:43], s[66:67], s[66:67] op_sel_hi:[1,0,0]
	global_store_dwordx2 v[40:41], v[38:39], off
	v_rcp_f32_e32 v42, v42
	v_pk_fma_f32 v[44:45], v[44:45], s[66:67], s[66:67] op_sel_hi:[1,0,0]
	v_pk_fma_f32 v[46:47], v[46:47], s[66:67], s[66:67] op_sel_hi:[1,0,0]
	v_rcp_f32_e32 v43, v43
	v_pk_fma_f32 v[48:49], v[48:49], s[66:67], s[66:67] op_sel_hi:[1,0,0]
	v_rcp_f32_e32 v44, v44
	v_rcp_f32_e32 v45, v45
	v_rcp_f32_e32 v46, v46
	v_pk_mul_f32 v[42:43], v[78:79], v[42:43]
	v_rcp_f32_e32 v47, v47
	v_pk_mul_f32 v[42:43], v[42:43], v[74:75]
	v_pk_mul_f32 v[44:45], v[80:81], v[44:45]
	v_rcp_f32_e32 v48, v48
	v_pk_mul_f32 v[44:45], v[44:45], v[76:77]
	v_pk_mul_f32 v[46:47], v[70:71], v[46:47]
	v_rcp_f32_e32 v49, v49
	v_pk_mul_f32 v[46:47], v[46:47], v[66:67]
	v_med3_f32 v42, v42, s29, v1
	v_med3_f32 v43, v43, s29, v1
	v_med3_f32 v44, v44, s29, v1
	v_pk_mul_f32 v[48:49], v[72:73], v[48:49]
	v_med3_f32 v45, v45, s29, v1
	v_pk_mul_f32 v[48:49], v[48:49], v[68:69]
	v_med3_f32 v46, v46, s29, v1
	v_med3_f32 v47, v47, s29, v1
	v_med3_f32 v48, v48, s29, v1
	v_med3_f32 v49, v49, s29, v1
	v_cvt_pk_fp8_f32 v50, v42, v43
	v_cvt_pk_fp8_f32 v51, v46, v47
	v_cvt_pk_fp8_f32 v50, v44, v45 op_sel:[0,0,1]
	v_cvt_pk_fp8_f32 v51, v48, v49 op_sel:[0,0,1]
	s_nop 0
	global_store_dwordx2 v[52:53], v[50:51], off
	s_mov_b64 s[38:39], -1
	s_cbranch_vccnz .LBB0_1362
	s_andn2_b64 vcc, exec, s[80:81]
	s_cbranch_vccnz .LBB0_1361
	s_barrier
	s_branch .LBB0_1361
